# residual epilogues (P9/P12/P20) hand-scheduled with global ops and counted waits; 4-way start stagger (s_sleep) of the workgroups that have one GEMM unit fewer in P9/P12 so epilogue bursts interleave
# speedup vs baseline: 1.0025x; 1.0025x over previous
.LBB0_1169:
.LBB0_1170:
	s_cmp_lt_i32 s26, 32
	s_cbranch_scc1 .Lstag9_done
	s_and_b32 s98, s26, 3
	s_mul_i32 s98, s98, 3
	s_cmp_eq_u32 s98, 0
	s_cbranch_scc1 .Lstag9_done
.Lstag9_loop:
	s_sleep 127
	s_add_i32 s98, s98, -1
	s_cmp_lg_u32 s98, 0
	s_cbranch_scc1 .Lstag9_loop

.LBB0_1589:
.LBB0_1590:
	s_cmp_lt_i32 s26, 32
	s_cbranch_scc1 .Lstag12_done
	s_and_b32 s98, s26, 3
	s_mul_i32 s98, s98, 4
	s_cmp_eq_u32 s98, 0
	s_cbranch_scc1 .Lstag12_done
